# speedup vs baseline: 1.0148x; 1.0148x over previous
.LBB1_5:
	s_andn2_saveexec_b64 s[4:5], s[4:5]
	s_cbranch_execz .LBB1_17
	s_load_dwordx2 s[8:9], s[0:1], 0x28
	s_load_dwordx2 s[10:11], s[0:1], 0x38
	s_load_dwordx2 s[12:13], s[0:1], 0x40
	s_load_dwordx2 s[14:15], s[0:1], 0x48
	s_load_dwordx2 s[16:17], s[0:1], 0x50
	s_load_dwordx2 s[18:19], s[0:1], 0x58
	s_load_dwordx2 s[20:21], s[0:1], 0x60
	s_load_dwordx2 s[22:23], s[0:1], 0x68
	s_mov_b64 s[24:25], exec
	s_mov_b32 s6, 0xaaaaaaab
	v_mul_hi_u32 v3, v2, s6
	v_lshrrev_b32_e32 v3, 3, v3
	v_mul_u32_u24_e32 v4, 12, v3
	v_sub_u32_e32 v4, v2, v4
	v_lshlrev_b32_e32 v5, 2, v3
	v_cmp_gt_u32_e64 s[26:27], 8, v4
	v_cmp_gt_u32_e64 s[28:29], 10, v4
	v_cmp_eq_u32_e64 s[30:31], 10, v4
	v_mov_b32_e32 v8, 0
	v_mov_b32_e32 v9, 0
	v_mov_b32_e32 v10, 0
	v_mov_b32_e32 v11, 0
	v_mov_b32_e32 v12, 0
	v_mov_b32_e32 v13, 0
	v_mov_b32_e32 v14, 0
	v_mov_b32_e32 v15, 0
	s_andn2_b64 s[28:29], s[28:29], s[26:27]
	s_and_b64 s[26:27], s[26:27], s[24:25]
	s_and_b64 s[28:29], s[28:29], s[24:25]
	s_and_b64 s[30:31], s[30:31], s[24:25]
	s_waitcnt lgkmcnt(0)
	s_mov_b64 exec, s[28:29]
	s_cbranch_execz .Ltbc_np
	global_load_dword v6, v5, s[10:11]
.Ltbc_np:
	s_mov_b64 exec, s[30:31]
	s_cbranch_execz .Ltbc_nf
	global_load_dword v6, v5, s[12:13]
	global_load_dword v7, v5, s[14:15]
.Ltbc_nf:
	s_mov_b64 exec, s[24:25]
	v_lshlrev_b32_e32 v16, 8, v3
	v_lshl_add_u32 v16, v4, 5, v16
	v_mul_u32_u24_e32 v17, 0xc0, v3
	v_lshl_add_u32 v17, v4, 4, v17
	s_waitcnt vmcnt(0)
	s_mov_b64 exec, s[26:27]
	s_cbranch_execz .Ltbc_nr
	global_load_dwordx4 v[8:11], v16, s[8:9] nt
	global_load_dwordx4 v[12:15], v16, s[8:9] offset:16 nt
.Ltbc_nr:
	s_mov_b64 exec, s[28:29]
	s_cbranch_execz .Ltbc_ne
	v_lshlrev_b32_e32 v18, 6, v6
	v_lshl_add_u32 v18, v4, 5, v18
	v_add_u32_e32 v18, 0xffffff00, v18
	global_load_dwordx4 v[8:11], v18, s[16:17]
	global_load_dwordx4 v[12:15], v18, s[16:17] offset:16
.Ltbc_ne:
	s_mov_b64 exec, s[30:31]
	s_cbranch_execz .Ltbc_ng
	v_lshlrev_b32_e32 v18, 3, v6
	v_lshlrev_b32_e32 v19, 3, v7
	global_load_dwordx2 v[8:9], v18, s[18:19]
	global_load_dwordx2 v[10:11], v19, s[20:21]
.Ltbc_ng:
	s_mov_b64 exec, s[24:25]
	s_waitcnt vmcnt(0)
	v_cvt_pk_f16_f32 v8, v8, v9
	v_cvt_pk_f16_f32 v9, v10, v11
	v_cvt_pk_f16_f32 v10, v12, v13
	v_cvt_pk_f16_f32 v11, v14, v15
	global_store_dwordx4 v17, v[8:11], s[22:23] sc1
	s_nop 1

	.amdhsa_kernel _Z8k_bcountPKiS0_S0_PiPjPKfS4_S0_S0_S0_S4_S4_S4_PDF16_S5_
		.amdhsa_group_segment_fixed_size 4384
		.amdhsa_private_segment_fixed_size 0
		.amdhsa_kernarg_size 120
		.amdhsa_user_sgpr_count 2
		.amdhsa_user_sgpr_dispatch_ptr 0
		.amdhsa_user_sgpr_queue_ptr 0
		.amdhsa_user_sgpr_kernarg_segment_ptr 1
		.amdhsa_user_sgpr_dispatch_id 0
		.amdhsa_user_sgpr_kernarg_preload_length 0
		.amdhsa_user_sgpr_kernarg_preload_offset 0
		.amdhsa_user_sgpr_private_segment_size 0
		.amdhsa_uses_dynamic_stack 0
		.amdhsa_enable_private_segment 0
		.amdhsa_system_sgpr_workgroup_id_x 1
		.amdhsa_system_sgpr_workgroup_id_y 0
		.amdhsa_system_sgpr_workgroup_id_z 0
		.amdhsa_system_sgpr_workgroup_info 0
		.amdhsa_system_vgpr_workitem_id 0
		.amdhsa_next_free_vgpr 41
		.amdhsa_next_free_sgpr 40
		.amdhsa_accum_offset 44
		.amdhsa_reserve_vcc 1
		.amdhsa_float_round_mode_32 0
		.amdhsa_float_round_mode_16_64 0
		.amdhsa_float_denorm_mode_32 3
		.amdhsa_float_denorm_mode_16_64 3
		.amdhsa_dx10_clamp 1
		.amdhsa_ieee_mode 1
		.amdhsa_fp16_overflow 0
		.amdhsa_tg_split 0
		.amdhsa_exception_fp_ieee_invalid_op 0
		.amdhsa_exception_fp_denorm_src 0
		.amdhsa_exception_fp_ieee_div_zero 0
		.amdhsa_exception_fp_ieee_overflow 0
		.amdhsa_exception_fp_ieee_underflow 0
		.amdhsa_exception_fp_ieee_inexact 0
		.amdhsa_exception_int_div_zero 0
	.end_amdhsa_kernel

.LBB2_118:
	s_andn2_saveexec_b64 s[4:5], s[4:5]
	s_cbranch_execz .LBB2_130
	s_load_dwordx2 s[8:9], s[0:1], 0x30
	s_load_dwordx2 s[10:11], s[0:1], 0x40
	s_load_dwordx2 s[12:13], s[0:1], 0x48
	s_load_dwordx2 s[14:15], s[0:1], 0x50
	s_load_dwordx2 s[16:17], s[0:1], 0x58
	s_load_dwordx2 s[18:19], s[0:1], 0x60
	s_load_dwordx2 s[20:21], s[0:1], 0x68
	s_load_dwordx2 s[22:23], s[0:1], 0x70
	s_mov_b64 s[24:25], exec
	s_mov_b32 s6, 0xaaaaaaab
	v_mul_hi_u32 v3, v2, s6
	v_lshrrev_b32_e32 v3, 3, v3
	v_mul_u32_u24_e32 v4, 12, v3
	v_sub_u32_e32 v4, v2, v4
	v_lshlrev_b32_e32 v5, 2, v3
	v_cmp_gt_u32_e64 s[26:27], 8, v4
	v_cmp_gt_u32_e64 s[28:29], 10, v4
	v_cmp_eq_u32_e64 s[30:31], 10, v4
	v_mov_b32_e32 v8, 0
	v_mov_b32_e32 v9, 0
	v_mov_b32_e32 v10, 0
	v_mov_b32_e32 v11, 0
	v_mov_b32_e32 v12, 0
	v_mov_b32_e32 v13, 0
	v_mov_b32_e32 v14, 0
	v_mov_b32_e32 v15, 0
	s_andn2_b64 s[28:29], s[28:29], s[26:27]
	s_and_b64 s[26:27], s[26:27], s[24:25]
	s_and_b64 s[28:29], s[28:29], s[24:25]
	s_and_b64 s[30:31], s[30:31], s[24:25]
	s_waitcnt lgkmcnt(0)
	s_mov_b64 exec, s[28:29]
	s_cbranch_execz .Ltpr_np
	global_load_dword v6, v5, s[10:11]

	.amdhsa_kernel _Z6k_prepPKiS0_S0_S0_PiP15HIP_vector_typeIiLj2EEPKfS6_S0_S0_S0_S6_S6_S6_PDF16_S7_6WSpecs
		.amdhsa_group_segment_fixed_size 17024
		.amdhsa_private_segment_fixed_size 0
		.amdhsa_kernarg_size 616
		.amdhsa_user_sgpr_count 2
		.amdhsa_user_sgpr_dispatch_ptr 0
		.amdhsa_user_sgpr_queue_ptr 0
		.amdhsa_user_sgpr_kernarg_segment_ptr 1
		.amdhsa_user_sgpr_dispatch_id 0
		.amdhsa_user_sgpr_kernarg_preload_length 0
		.amdhsa_user_sgpr_kernarg_preload_offset 0
		.amdhsa_user_sgpr_private_segment_size 0
		.amdhsa_uses_dynamic_stack 0
		.amdhsa_enable_private_segment 0
		.amdhsa_system_sgpr_workgroup_id_x 1
		.amdhsa_system_sgpr_workgroup_id_y 0
		.amdhsa_system_sgpr_workgroup_id_z 0
		.amdhsa_system_sgpr_workgroup_info 0
		.amdhsa_system_vgpr_workitem_id 0
		.amdhsa_next_free_vgpr 82
		.amdhsa_next_free_sgpr 40
		.amdhsa_accum_offset 84
		.amdhsa_reserve_vcc 1
		.amdhsa_float_round_mode_32 0
		.amdhsa_float_round_mode_16_64 0
		.amdhsa_float_denorm_mode_32 3
		.amdhsa_float_denorm_mode_16_64 3
		.amdhsa_dx10_clamp 1
		.amdhsa_ieee_mode 1
		.amdhsa_fp16_overflow 0
		.amdhsa_tg_split 0
		.amdhsa_exception_fp_ieee_invalid_op 0
		.amdhsa_exception_fp_denorm_src 0
		.amdhsa_exception_fp_ieee_div_zero 0
		.amdhsa_exception_fp_ieee_overflow 0
		.amdhsa_exception_fp_ieee_underflow 0
		.amdhsa_exception_fp_ieee_inexact 0
		.amdhsa_exception_int_div_zero 0
	.end_amdhsa_kernel
